# P3 counted waits for in-flight weight-conversion loads; P9 sink wait moved ahead of next-item prefetch; P4 elem-first waves load next operands straight into their final registers (no copies / vmcnt(0)
# speedup vs baseline: 1.0088x; 1.0088x over previous
.LBB0_433:
	s_or_b64 exec, exec, s[0:1]
	v_lshrrev_b32_e32 v80, 3, v84
	v_mul_lo_u32 v81, v80, s60
	v_lshlrev_b32_e32 v80, 4, v84
	v_and_b32_e32 v82, 0x70, v80
	v_add3_u32 v81, s78, v81, v82
	s_cmp_gt_u32 s74, 5
	s_waitcnt vmcnt(3)
	ds_write_b128 v81, v[172:175] offset:53248
	s_waitcnt vmcnt(2)
	ds_write_b128 v81, v[176:179] offset:62464
	s_cbranch_scc1 .LBB0_435
	v_and_b32_e32 v10, 0xffffffc0, v80
	v_ashrrev_i32_e32 v11, 31, v10
	v_lshlrev_b64 v[10:11], 1, v[10:11]
	s_add_u32 s0, s75, s22
	v_lshl_or_b32 v10, v0, 5, v10
	s_addc_u32 s1, s77, s23
	v_lshl_add_u64 v[80:81], s[0:1], 0, v[10:11]
	v_add_co_u32_e32 v12, vcc, s65, v80
	v_lshl_add_u64 v[10:11], v[80:81], 0, s[14:15]
	s_nop 0
	v_addc_co_u32_e32 v13, vcc, 0, v81, vcc
	v_lshl_add_u64 v[82:83], v[80:81], 0, s[16:17]
	v_add_co_u32_e32 v80, vcc, s66, v80
	v_ashrrev_i32_e32 v85, 31, v84
	s_nop 0
	v_addc_co_u32_e32 v81, vcc, 0, v81, vcc
	global_load_dwordx4 v[180:183], v[12:13], off
	s_nop 0
	global_load_dwordx4 v[188:191], v[10:11], off offset:16
	s_nop 0
	global_load_dwordx4 v[192:195], v[80:81], off
	global_load_dwordx4 v[184:187], v[82:83], off offset:16
	v_lshl_add_u64 v[80:81], v[84:85], 4, s[0:1]
	v_add_co_u32_e32 v82, vcc, 0x26240000, v80
	s_nop 1
	v_addc_co_u32_e32 v83, vcc, 0, v81, vcc
	v_add_co_u32_e32 v80, vcc, 0x26242000, v80
	s_nop 1
	v_addc_co_u32_e32 v81, vcc, 0, v81, vcc
	global_load_dwordx4 v[200:203], v[82:83], off
	global_load_dwordx4 v[196:199], v[80:81], off
.LBB0_435:
	v_mov_b32_e32 v0, v214
	v_and_b32_e32 v164, 31, v0
	v_bfe_u32 v165, v0, 5, 1
	v_or_b32_e32 v0, s37, v164
	v_mov_b32_e32 v10, s76
	v_mad_u32_u24 v135, v0, s64, v10
	v_lshlrev_b32_e32 v133, 4, v165
	v_add_u32_e32 v10, v135, v133
	ds_read_b128 v[120:123], v10
	ds_read_b128 v[116:119], v10 offset:32
	ds_read_b128 v[112:115], v10 offset:64
	ds_read_b128 v[108:111], v10 offset:96
	ds_read_b128 v[104:107], v10 offset:128
	ds_read_b128 v[100:103], v10 offset:160
	ds_read_b128 v[96:99], v10 offset:192
	ds_read_b128 v[10:13], v10 offset:224
	v_or_b32_e32 v80, s8, v164
	v_mul_lo_u32 v80, v80, s60
	v_add_u32_e32 v134, s76, v80
	v_lshlrev_b32_e32 v166, 3, v165
	v_add_u32_e32 v132, s76, v133
	v_add_u32_e32 v124, v134, v166
	s_mov_b64 s[0:1], -1
	s_and_b64 vcc, exec, s[10:11]
	s_cbranch_vccz .LBB0_443
	v_mad_u32_u24 v84, v164, s64, v132
	ds_read_b128 v[80:83], v84 offset:17408
	ds_read_b128 v[126:129], v84 offset:17440
	ds_read_b128 v[136:139], v84 offset:17472
	ds_read_b128 v[140:143], v84 offset:17504
	ds_read_b128 v[144:147], v84 offset:17536
	ds_read_b128 v[148:151], v84 offset:17568
	ds_read_b128 v[152:155], v84 offset:17600
	ds_read_b128 v[156:159], v84 offset:17632
	v_add_u32_e32 v84, 0xd000, v124
	ds_read2_b64 v[160:163], v84 offset1:2
	ds_read2_b64 v[168:171], v84 offset0:4 offset1:6
	s_waitcnt lgkmcnt(0)
	s_waitcnt lgkmcnt(9)
	v_mfma_f32_32x32x16_bf16 v[80:95], v[80:83], v[120:123], 0
	s_waitcnt lgkmcnt(8)
	v_mfma_f32_32x32x16_bf16 v[80:95], v[126:129], v[116:119], v[80:95]
	s_waitcnt lgkmcnt(7)
	v_mfma_f32_32x32x16_bf16 v[80:95], v[136:139], v[112:115], v[80:95]
	s_waitcnt lgkmcnt(6)
	v_mfma_f32_32x32x16_bf16 v[80:95], v[140:143], v[108:111], v[80:95]
	s_waitcnt lgkmcnt(5)
	v_mfma_f32_32x32x16_bf16 v[80:95], v[144:147], v[104:107], v[80:95]
	s_waitcnt lgkmcnt(4)
	v_mfma_f32_32x32x16_bf16 v[80:95], v[148:151], v[100:103], v[80:95]
	s_waitcnt lgkmcnt(3)
	v_mfma_f32_32x32x16_bf16 v[80:95], v[152:155], v[96:99], v[80:95]
	s_waitcnt lgkmcnt(2)
	v_mfma_f32_32x32x16_bf16 v[80:95], v[156:159], v[10:13], v[80:95]
	s_nop 11
	v_cvt_pk_bf16_f32 v80, v80, v81
	v_cvt_pk_bf16_f32 v81, v82, v83
	v_cvt_pk_bf16_f32 v82, v84, v85
	v_cvt_pk_bf16_f32 v83, v86, v87
	s_waitcnt lgkmcnt(1)
	s_nop 0
	v_mfma_f32_32x32x16_bf16 v[144:159], v[160:163], v[80:83], 0
	v_cvt_pk_bf16_f32 v80, v88, v89
	v_cvt_pk_bf16_f32 v81, v90, v91
	v_cvt_pk_bf16_f32 v82, v92, v93
	v_cvt_pk_bf16_f32 v83, v94, v95
	s_waitcnt lgkmcnt(0)
	s_nop 0
	v_mfma_f32_32x32x16_bf16 v[144:159], v[168:171], v[80:83], v[144:159]
	s_mov_b32 s0, 1
	s_cbranch_execnz .LBB0_438

.LBB0_869:
	s_ashr_i32 s38, s37, 31
	s_lshr_b32 s2, s38, 25
	s_add_i32 s2, s37, s2
	s_ashr_i32 s39, s2, 7
	s_lshr_b32 s2, s39, 30
	s_add_i32 s2, s39, s2
	s_and_b32 s2, s2, 0x3ffffffc
	s_sub_i32 s2, s39, s2
	s_lshl_b32 s2, s2, 2
	s_or_b32 s8, s2, s22
	s_mul_i32 s2, s34, 0xd000
	s_ashr_i32 s9, s8, 31
	s_add_i32 s36, s2, 0
	s_add_i32 s35, s37, s72
	s_lshl_b64 s[2:3], s[8:9], 2
	s_add_u32 s2, s70, s2
	s_addc_u32 s3, s71, s3
	global_load_dword v156, v112, s[2:3]
	s_lshl_b32 s2, s8, 9
	s_add_i32 s2, s2, 0
	v_mov_b32_e32 v157, v123
	s_add_i32 s2, s2, 0x1a000
	v_add3_u32 v113, s36, v140, v144
	v_lshl_add_u32 v74, v157, 2, s2
	ds_read2_b32 v[2:3], v74 offset0:127 offset1:128
	ds_read2_b32 v[4:5], v74 offset0:125 offset1:126
	ds_read2_b32 v[6:7], v74 offset0:119 offset1:120
	ds_read2_b32 v[8:9], v74 offset0:117 offset1:118
	ds_read2_b32 v[10:11], v74 offset0:111 offset1:112
	ds_read2_b32 v[12:13], v74 offset0:109 offset1:110
	ds_read2_b32 v[14:15], v74 offset0:103 offset1:104
	ds_read2_b32 v[20:21], v74 offset0:101 offset1:102
	ds_read_b128 v[16:19], v113
	s_waitcnt lgkmcnt(8)
	v_mov_b32_e32 v0, v3
	v_mov_b32_e32 v1, v2
	s_waitcnt lgkmcnt(7)
	v_mov_b32_e32 v2, v5
	v_mov_b32_e32 v3, v4
	s_waitcnt lgkmcnt(6)
	v_mov_b32_e32 v4, v7
	v_mov_b32_e32 v5, v6
	s_waitcnt lgkmcnt(5)
	v_mov_b32_e32 v6, v9
	v_mov_b32_e32 v7, v8
	s_waitcnt lgkmcnt(4)
	v_mov_b32_e32 v8, v11
	v_mov_b32_e32 v9, v10
	s_waitcnt lgkmcnt(3)
	v_mov_b32_e32 v10, v13
	v_mov_b32_e32 v11, v12
	s_waitcnt lgkmcnt(2)
	v_mov_b32_e32 v12, v15
	v_mov_b32_e32 v13, v14
	s_waitcnt lgkmcnt(1)
	v_mov_b32_e32 v14, v21
	v_mov_b32_e32 v15, v20
	ds_read_b128 v[20:23], v113 offset:32
	v_subrev_u32_e32 v72, 44, v74
	s_waitcnt lgkmcnt(1)
	v_mfma_f32_32x32x16_bf16 v[0:15], v[16:19], v[92:95], v[0:15]
	v_add_u32_e32 v78, 0xffffff9c, v74
	v_add_u32_e32 v135, 0xffffff94, v74
	s_cmpk_lt_i32 s35, 0x1000
	s_cselect_b64 s[12:13], -1, 0
	s_cmpk_gt_i32 s35, 0xfff
	s_cselect_b64 s[10:11], -1, 0
	s_and_b64 vcc, exec, s[10:11]
	s_waitcnt lgkmcnt(0)
	v_mfma_f32_32x32x16_bf16 v[0:15], v[20:23], v[96:99], v[0:15]
	ds_read_b128 v[16:19], v113 offset:64
	ds_read_b128 v[20:23], v113 offset:96
	s_waitcnt lgkmcnt(1)
	v_mfma_f32_32x32x16_bf16 v[0:15], v[16:19], v[100:103], v[0:15]
	s_waitcnt lgkmcnt(0)
	v_mfma_f32_32x32x16_bf16 v[0:15], v[20:23], v[104:107], v[0:15]
	ds_read2_b32 v[18:19], v74 offset0:95 offset1:96
	ds_read2_b32 v[20:21], v74 offset0:93 offset1:94
	ds_read2_b32 v[22:23], v74 offset0:87 offset1:88
	ds_read2_b32 v[24:25], v74 offset0:85 offset1:86
	ds_read2_b32 v[26:27], v74 offset0:79 offset1:80
	ds_read2_b32 v[28:29], v74 offset0:77 offset1:78
	ds_read2_b32 v[30:31], v74 offset0:71 offset1:72
	ds_read2_b32 v[36:37], v74 offset0:69 offset1:70
	ds_read_b128 v[32:35], v113 offset:4608
	s_waitcnt lgkmcnt(8)
	v_mov_b32_e32 v16, v19
	v_mov_b32_e32 v17, v18
	s_waitcnt lgkmcnt(7)
	v_mov_b32_e32 v18, v21
	v_mov_b32_e32 v19, v20
	s_waitcnt lgkmcnt(6)
	v_mov_b32_e32 v20, v23
	v_mov_b32_e32 v21, v22
	s_waitcnt lgkmcnt(5)
	v_mov_b32_e32 v22, v25
	v_mov_b32_e32 v23, v24
	s_waitcnt lgkmcnt(4)
	v_mov_b32_e32 v24, v27
	v_mov_b32_e32 v25, v26
	s_waitcnt lgkmcnt(3)
	v_mov_b32_e32 v26, v29
	v_mov_b32_e32 v27, v28
	s_waitcnt lgkmcnt(2)
	v_mov_b32_e32 v28, v31
	v_mov_b32_e32 v29, v30
	s_waitcnt lgkmcnt(1)
	v_mov_b32_e32 v30, v37
	v_mov_b32_e32 v31, v36
	ds_read_b128 v[36:39], v113 offset:4640
	s_waitcnt lgkmcnt(1)
	v_mfma_f32_32x32x16_bf16 v[16:31], v[32:35], v[92:95], v[16:31]
	s_waitcnt lgkmcnt(0)
	v_mfma_f32_32x32x16_bf16 v[16:31], v[36:39], v[96:99], v[16:31]
	ds_read_b128 v[32:35], v113 offset:4672
	ds_read_b128 v[36:39], v113 offset:4704
	s_waitcnt lgkmcnt(1)
	v_mfma_f32_32x32x16_bf16 v[16:31], v[32:35], v[100:103], v[16:31]
	s_waitcnt lgkmcnt(0)
	v_mfma_f32_32x32x16_bf16 v[16:31], v[36:39], v[104:107], v[16:31]
	ds_read2_b32 v[34:35], v74 offset0:63 offset1:64
	ds_read2_b32 v[36:37], v74 offset0:61 offset1:62
	ds_read2_b32 v[38:39], v74 offset0:55 offset1:56
	ds_read2_b32 v[40:41], v74 offset0:53 offset1:54
	ds_read2_b32 v[42:43], v74 offset0:47 offset1:48
	ds_read2_b32 v[44:45], v74 offset0:45 offset1:46
	ds_read2_b32 v[46:47], v74 offset0:39 offset1:40
	ds_read2_b32 v[52:53], v74 offset0:37 offset1:38
	ds_read_b128 v[48:51], v113 offset:9216
	s_waitcnt lgkmcnt(8)
	v_mov_b32_e32 v32, v35
	v_mov_b32_e32 v33, v34
	s_waitcnt lgkmcnt(7)
	v_mov_b32_e32 v34, v37
	v_mov_b32_e32 v35, v36
	s_waitcnt lgkmcnt(6)
	v_mov_b32_e32 v36, v39
	v_mov_b32_e32 v37, v38
	s_waitcnt lgkmcnt(5)
	v_mov_b32_e32 v38, v41
	v_mov_b32_e32 v39, v40
	s_waitcnt lgkmcnt(4)
	v_mov_b32_e32 v40, v43
	v_mov_b32_e32 v41, v42
	s_waitcnt lgkmcnt(3)
	v_mov_b32_e32 v42, v45
	v_mov_b32_e32 v43, v44
	s_waitcnt lgkmcnt(2)
	v_mov_b32_e32 v44, v47
	v_mov_b32_e32 v45, v46
	s_waitcnt lgkmcnt(1)
	v_mov_b32_e32 v46, v53
	v_mov_b32_e32 v47, v52
	ds_read_b128 v[52:55], v113 offset:9248
	s_waitcnt lgkmcnt(1)
	v_mfma_f32_32x32x16_bf16 v[32:47], v[48:51], v[92:95], v[32:47]
	s_waitcnt lgkmcnt(0)
	v_mfma_f32_32x32x16_bf16 v[32:47], v[52:55], v[96:99], v[32:47]
	ds_read_b128 v[48:51], v113 offset:9280
	ds_read_b128 v[52:55], v113 offset:9312
	s_waitcnt lgkmcnt(1)
	v_mfma_f32_32x32x16_bf16 v[32:47], v[48:51], v[100:103], v[32:47]
	s_waitcnt lgkmcnt(0)
	v_mfma_f32_32x32x16_bf16 v[32:47], v[52:55], v[104:107], v[32:47]
	ds_read2_b32 v[50:51], v74 offset0:31 offset1:32
	ds_read2_b32 v[52:53], v74 offset0:29 offset1:30
	ds_read2_b32 v[54:55], v74 offset0:23 offset1:24
	ds_read2_b32 v[56:57], v74 offset0:21 offset1:22
	ds_read2_b32 v[58:59], v74 offset0:15 offset1:16
	ds_read2_b32 v[60:61], v74 offset0:13 offset1:14
	ds_read2_b32 v[62:63], v74 offset0:7 offset1:8
	ds_read2_b32 v[68:69], v74 offset0:5 offset1:6
	ds_read_b128 v[64:67], v113 offset:13824
	s_waitcnt lgkmcnt(8)
	v_mov_b32_e32 v48, v51
	v_mov_b32_e32 v49, v50
	s_waitcnt lgkmcnt(7)
	v_mov_b32_e32 v50, v53
	v_mov_b32_e32 v51, v52
	s_waitcnt lgkmcnt(6)
	v_mov_b32_e32 v52, v55
	v_mov_b32_e32 v53, v54
	s_waitcnt lgkmcnt(5)
	v_mov_b32_e32 v54, v57
	v_mov_b32_e32 v55, v56
	s_waitcnt lgkmcnt(4)
	v_mov_b32_e32 v56, v59
	v_mov_b32_e32 v57, v58
	s_waitcnt lgkmcnt(3)
	v_mov_b32_e32 v58, v61
	v_mov_b32_e32 v59, v60
	s_waitcnt lgkmcnt(2)
	v_mov_b32_e32 v60, v63
	v_mov_b32_e32 v61, v62
	s_waitcnt lgkmcnt(1)
	v_mov_b32_e32 v62, v69
	v_mov_b32_e32 v63, v68
	ds_read_b128 v[68:71], v113 offset:13856
	s_waitcnt lgkmcnt(1)
	v_mfma_f32_32x32x16_bf16 v[48:63], v[64:67], v[92:95], v[48:63]
	s_waitcnt lgkmcnt(0)
	v_mfma_f32_32x32x16_bf16 v[48:63], v[68:71], v[96:99], v[48:63]
	ds_read_b128 v[64:67], v113 offset:13888
	ds_read_b128 v[68:71], v113 offset:13920
	s_waitcnt lgkmcnt(1)
	v_mfma_f32_32x32x16_bf16 v[48:63], v[64:67], v[100:103], v[48:63]
	v_add_u32_e32 v64, -4, v74
	v_add_u32_e32 v65, -12, v74
	s_waitcnt lgkmcnt(0)
	v_mfma_f32_32x32x16_bf16 v[48:63], v[68:71], v[104:107], v[48:63]
	v_subrev_u32_e32 v70, 36, v74
	ds_read2_b32 v[66:67], v64 offset1:1
	ds_read2_b32 v[68:69], v65 offset1:1
	ds_read2_b32 v[70:71], v70 offset1:1
	ds_read2_b32 v[72:73], v72 offset1:1
	v_add_u32_e32 v64, 0xffffffbc, v74
	v_add_u32_e32 v65, 0xffffffb4, v74
	ds_read2_b32 v[74:75], v64 offset1:1
	ds_read2_b32 v[76:77], v65 offset1:1
	ds_read2_b32 v[78:79], v78 offset1:1
	ds_read2_b32 v[138:139], v135 offset1:1
	ds_read_b128 v[158:161], v113 offset:18432
	ds_read_b128 v[162:165], v113 offset:18464
	s_waitcnt lgkmcnt(9)
	v_mov_b32_e32 v64, v67
	v_mov_b32_e32 v65, v66
	s_waitcnt lgkmcnt(8)
	v_mov_b32_e32 v66, v69
	v_mov_b32_e32 v67, v68
	s_waitcnt lgkmcnt(7)
	v_mov_b32_e32 v68, v71
	v_mov_b32_e32 v69, v70
	s_waitcnt lgkmcnt(6)
	v_mov_b32_e32 v70, v73
	v_mov_b32_e32 v71, v72
	s_waitcnt lgkmcnt(5)
	v_mov_b32_e32 v72, v75
	v_mov_b32_e32 v73, v74
	s_waitcnt lgkmcnt(4)
	v_mov_b32_e32 v74, v77
	v_mov_b32_e32 v75, v76
	s_waitcnt lgkmcnt(3)
	v_mov_b32_e32 v76, v79
	v_mov_b32_e32 v77, v78
	s_waitcnt lgkmcnt(2)
	v_mov_b32_e32 v78, v139
	v_mov_b32_e32 v79, v138
	s_waitcnt lgkmcnt(1)
	s_nop 0
	v_mfma_f32_32x32x16_bf16 v[64:79], v[158:161], v[92:95], v[64:79]
	s_waitcnt lgkmcnt(0)
	v_mfma_f32_32x32x16_bf16 v[64:79], v[162:165], v[96:99], v[64:79]
	ds_read_b128 v[158:161], v113 offset:18496
	ds_read_b128 v[162:165], v113 offset:18528
	s_waitcnt lgkmcnt(1)
	v_mfma_f32_32x32x16_bf16 v[64:79], v[158:161], v[100:103], v[64:79]
	s_waitcnt lgkmcnt(0)
	v_mfma_f32_32x32x16_bf16 v[64:79], v[162:165], v[104:107], v[64:79]
	s_waitcnt vmcnt(0)
	s_cbranch_vccnz .LBB0_885
	s_ashr_i32 s2, s35, 31
	s_lshr_b32 s3, s2, 23
	s_lshr_b32 s2, s2, 25
	s_add_i32 s2, s35, s2
	s_ashr_i32 s6, s2, 7
	s_add_i32 s3, s35, s3
	s_lshr_b32 s2, s6, 30
	s_ashr_i32 s14, s3, 9
	s_add_i32 s2, s6, s2
	s_lshl_b32 s9, s6, 13
	s_add_i32 s17, s23, s30
	s_and_b32 s2, s2, -4
	s_ashr_i32 s15, s14, 31
	s_sub_i32 s17, s17, s9
	s_sub_i32 s16, s6, s2
	s_lshl_b64 s[2:3], s[14:15], 13
	s_ashr_i32 s40, s17, 31
	s_add_u32 s2, s2, s17
	s_addc_u32 s3, s3, s40
	v_mov_b32_e32 v81, s3
	v_or_b32_e32 v80, s2, v122
	s_lshl_b32 s2, s16, 8
	v_lshlrev_b64 v[80:81], 11, v[80:81]
	s_or_b32 s2, s2, s26
	v_lshl_add_u64 v[80:81], s[4:5], 0, v[80:81]
	s_ashr_i32 s3, s2, 31
	v_lshl_add_u64 v[80:81], s[2:3], 1, v[80:81]
	v_mov_b32_e32 v135, v112
	v_lshl_add_u64 v[80:81], v[80:81], 0, v[134:135]
	global_load_dwordx4 v[92:95], v[80:81], off
	global_load_dwordx4 v[96:99], v[80:81], off offset:32
	global_load_dwordx4 v[100:103], v[80:81], off offset:64
	global_load_dwordx4 v[104:107], v[80:81], off offset:96
	s_lshl_b64 s[2:3], s[14:15], 22
	s_add_u32 s40, s18, s2
	s_addc_u32 s41, s19, s3
	s_lshl_b32 s16, s16, 6
	s_ashr_i32 s17, s16, 31
	s_lshl_b64 s[2:3], s[16:17], 1
	s_add_u32 s2, s40, s2
	s_addc_u32 s3, s41, s3
	v_mov_b32_e32 v137, v112
	v_lshl_add_u64 v[118:119], s[2:3], 0, v[136:137]
	s_sub_i32 s2, s30, s9
	v_mov_b32_e32 v113, v112
	v_add_u32_e32 v84, s2, v152
	v_mov_b32_e32 v114, v112
	v_mov_b32_e32 v115, v112
	v_mov_b64_e32 v[80:81], v[112:113]
	v_cmp_lt_i32_e32 vcc, -1, v84
	v_mov_b64_e32 v[82:83], v[114:115]
	s_and_saveexec_b64 s[2:3], vcc
	s_cbranch_execz .LBB0_872
	v_mov_b32_e32 v85, v112
	v_lshlrev_b64 v[80:81], 9, v[84:85]
	v_lshl_add_u64 v[80:81], v[118:119], 0, v[80:81]
	global_load_dwordx4 v[80:83], v[80:81], off

.LBB0_885:
	s_lshl_b32 s2, s39, 13
	s_sub_i32 s14, s27, s2
	s_add_i32 s6, s29, s2
	s_lshr_b32 s2, s38, 23
	s_add_i32 s2, s37, s2
	s_ashr_i32 s16, s2, 9
	v_cmp_gt_i32_e64 s[2:3], 1, v157
	s_ashr_i32 s17, s16, 31
	s_cmpk_lt_i32 s14, 0x80
	v_cndmask_b32_e64 v1, v155, v1, s[2:3]
	v_cmp_gt_i32_e64 s[2:3], 2, v157
	v_cmp_gt_i32_e32 vcc, 0, v157
	v_mul_f32_e32 v113, 0x3fb8aa3b, v156
	v_cndmask_b32_e64 v2, v155, v2, s[2:3]
	v_cmp_gt_i32_e64 s[2:3], 3, v157
	v_cndmask_b32_e32 v0, v155, v0, vcc
	s_cselect_b64 vcc, -1, 0
	v_cndmask_b32_e64 v3, v155, v3, s[2:3]
	v_cmp_gt_i32_e64 s[2:3], 8, v157
	v_cndmask_b32_e32 v0, v0, v155, vcc
	v_cndmask_b32_e32 v1, v1, v155, vcc
	v_cndmask_b32_e64 v4, v155, v4, s[2:3]
	v_cmp_gt_i32_e64 s[2:3], 9, v157
	v_max3_f32 v113, v113, v0, v1
	v_cndmask_b32_e32 v2, v2, v155, vcc
	v_cndmask_b32_e64 v5, v155, v5, s[2:3]
	v_cmp_gt_i32_e64 s[2:3], 10, v157
	v_cndmask_b32_e32 v3, v3, v155, vcc
	v_max3_f32 v113, v113, v2, v3
	v_cndmask_b32_e64 v6, v155, v6, s[2:3]
	v_cmp_gt_i32_e64 s[2:3], 11, v157
	v_cndmask_b32_e32 v4, v4, v155, vcc
	v_cndmask_b32_e32 v5, v5, v155, vcc
	v_cndmask_b32_e64 v7, v155, v7, s[2:3]
	v_cmp_gt_i32_e64 s[2:3], 16, v157
	v_max3_f32 v113, v113, v4, v5
	v_cndmask_b32_e32 v6, v6, v155, vcc
	v_cndmask_b32_e64 v8, v155, v8, s[2:3]
	v_cmp_gt_i32_e64 s[2:3], 17, v157
	v_cndmask_b32_e32 v7, v7, v155, vcc
	v_max3_f32 v113, v113, v6, v7
	v_cndmask_b32_e64 v9, v155, v9, s[2:3]
	v_cmp_gt_i32_e64 s[2:3], 18, v157
	v_cndmask_b32_e32 v8, v8, v155, vcc
	v_cndmask_b32_e32 v9, v9, v155, vcc
	v_cndmask_b32_e64 v10, v155, v10, s[2:3]
	v_cmp_gt_i32_e64 s[2:3], 19, v157
	v_max3_f32 v113, v113, v8, v9
	v_cndmask_b32_e32 v10, v10, v155, vcc
	v_cndmask_b32_e64 v11, v155, v11, s[2:3]
	v_cmp_gt_i32_e64 s[2:3], 24, v157
	v_cndmask_b32_e32 v11, v11, v155, vcc
	s_cmp_gt_u32 s6, 32
	v_cndmask_b32_e64 v12, v155, v12, s[2:3]
	v_cmp_gt_i32_e64 s[2:3], 25, v157
	v_max3_f32 v113, v113, v10, v11
	v_cndmask_b32_e32 v12, v12, v155, vcc
	v_cndmask_b32_e64 v13, v155, v13, s[2:3]
	v_cmp_gt_i32_e64 s[2:3], 26, v157
	v_cndmask_b32_e32 v13, v13, v155, vcc
	v_max3_f32 v113, v113, v12, v13
	v_cndmask_b32_e64 v14, v155, v14, s[2:3]
	v_cmp_gt_i32_e64 s[2:3], 27, v157
	v_cndmask_b32_e32 v14, v14, v155, vcc
	s_nop 0
	v_cndmask_b32_e64 v15, v155, v15, s[2:3]
	s_cselect_b64 s[2:3], -1, 0
	v_cndmask_b32_e32 v15, v15, v155, vcc
	s_and_b64 s[2:3], vcc, s[2:3]
	v_max3_f32 v113, v113, v14, v15
	v_cndmask_b32_e64 v16, v16, v155, s[2:3]
	v_cndmask_b32_e64 v17, v17, v155, s[2:3]
	v_max3_f32 v113, v113, v16, v17
	v_cndmask_b32_e64 v18, v18, v155, s[2:3]
	v_cndmask_b32_e64 v19, v19, v155, s[2:3]
	v_max3_f32 v113, v113, v18, v19
	v_cndmask_b32_e64 v20, v20, v155, s[2:3]
	v_cndmask_b32_e64 v21, v21, v155, s[2:3]
	v_max3_f32 v113, v113, v20, v21
	v_cndmask_b32_e64 v22, v22, v155, s[2:3]
	v_cndmask_b32_e64 v23, v23, v155, s[2:3]
	v_max3_f32 v113, v113, v22, v23
	v_cndmask_b32_e64 v24, v24, v155, s[2:3]
	v_cndmask_b32_e64 v25, v25, v155, s[2:3]
	v_max3_f32 v113, v113, v24, v25
	v_cndmask_b32_e64 v26, v26, v155, s[2:3]
	v_cndmask_b32_e64 v27, v27, v155, s[2:3]
	s_cmp_gt_u32 s6, 64
	v_max3_f32 v113, v113, v26, v27
	v_cndmask_b32_e64 v28, v28, v155, s[2:3]
	v_cndmask_b32_e64 v29, v29, v155, s[2:3]
	v_cndmask_b32_e64 v30, v30, v155, s[2:3]
	v_cndmask_b32_e64 v31, v31, v155, s[2:3]
	s_cselect_b64 s[2:3], -1, 0
	v_max3_f32 v113, v113, v28, v29
	s_and_b64 s[2:3], vcc, s[2:3]
	v_max3_f32 v113, v113, v30, v31
	v_cndmask_b32_e64 v135, v32, v155, s[2:3]
	v_cndmask_b32_e64 v137, v33, v155, s[2:3]
	v_max3_f32 v32, v113, v135, v137
	v_cndmask_b32_e64 v113, v34, v155, s[2:3]
	v_cndmask_b32_e64 v138, v35, v155, s[2:3]
	v_max3_f32 v32, v32, v113, v138
	v_cndmask_b32_e64 v139, v36, v155, s[2:3]
	v_cndmask_b32_e64 v158, v37, v155, s[2:3]
	v_max3_f32 v32, v32, v139, v158
	v_cndmask_b32_e64 v159, v38, v155, s[2:3]
	v_cndmask_b32_e64 v160, v39, v155, s[2:3]
	s_cmpk_gt_u32 s6, 0x60
	v_max3_f32 v32, v32, v159, v160
	v_cndmask_b32_e64 v161, v40, v155, s[2:3]
	v_cndmask_b32_e64 v162, v41, v155, s[2:3]
	v_cndmask_b32_e64 v163, v42, v155, s[2:3]
	v_cndmask_b32_e64 v164, v43, v155, s[2:3]
	v_cndmask_b32_e64 v165, v44, v155, s[2:3]
	v_cndmask_b32_e64 v166, v45, v155, s[2:3]
	v_cndmask_b32_e64 v167, v46, v155, s[2:3]
	v_cndmask_b32_e64 v168, v47, v155, s[2:3]
	s_cselect_b64 s[2:3], -1, 0
	v_max3_f32 v32, v32, v161, v162
	s_and_b64 vcc, vcc, s[2:3]
	v_max3_f32 v32, v32, v163, v164
	v_cndmask_b32_e32 v169, v48, v155, vcc
	v_cndmask_b32_e32 v170, v49, v155, vcc
	v_cndmask_b32_e32 v171, v50, v155, vcc
	v_cndmask_b32_e32 v172, v51, v155, vcc
	v_cndmask_b32_e32 v52, v52, v155, vcc
	v_cndmask_b32_e32 v53, v53, v155, vcc
	v_cndmask_b32_e32 v54, v54, v155, vcc
	v_cndmask_b32_e32 v55, v55, v155, vcc
	v_cndmask_b32_e32 v56, v56, v155, vcc
	v_cndmask_b32_e32 v173, v57, v155, vcc
	v_cndmask_b32_e32 v174, v58, v155, vcc
	v_cndmask_b32_e32 v175, v59, v155, vcc
	v_cndmask_b32_e32 v176, v60, v155, vcc
	v_cndmask_b32_e32 v51, v61, v155, vcc
	v_cndmask_b32_e32 v50, v62, v155, vcc
	v_cndmask_b32_e32 v48, v63, v155, vcc
	s_cmp_lt_i32 s14, 0
	v_cmp_lt_i32_e32 vcc, -1, v157
	v_max3_f32 v32, v32, v165, v166
	v_cmp_lt_i32_e64 s[2:3], 0, v157
	v_cndmask_b32_e32 v33, v155, v64, vcc
	s_cselect_b64 vcc, -1, 0
	v_max3_f32 v32, v32, v167, v168
	v_cndmask_b32_e32 v49, v33, v155, vcc
	v_cndmask_b32_e64 v33, v155, v65, s[2:3]
	v_cmp_lt_i32_e64 s[2:3], 1, v157
	v_max3_f32 v32, v32, v169, v170
	v_cndmask_b32_e32 v45, v33, v155, vcc
	v_cndmask_b32_e64 v33, v155, v66, s[2:3]
	v_cmp_lt_i32_e64 s[2:3], 2, v157
	v_max3_f32 v32, v32, v171, v172
	v_cndmask_b32_e32 v46, v33, v155, vcc
	v_cndmask_b32_e64 v33, v155, v67, s[2:3]
	v_cmp_lt_i32_e64 s[2:3], 7, v157
	v_max3_f32 v32, v32, v52, v53
	v_cndmask_b32_e32 v47, v33, v155, vcc
	v_cndmask_b32_e64 v33, v155, v68, s[2:3]
	v_cmp_lt_i32_e64 s[2:3], 8, v157
	v_max3_f32 v32, v32, v54, v55
	v_cndmask_b32_e32 v44, v33, v155, vcc
	v_cndmask_b32_e64 v33, v155, v69, s[2:3]
	v_cmp_lt_i32_e64 s[2:3], 9, v157
	v_max3_f32 v32, v32, v56, v173
	v_cndmask_b32_e32 v43, v33, v155, vcc
	v_cndmask_b32_e64 v33, v155, v70, s[2:3]
	v_cmp_lt_i32_e64 s[2:3], 10, v157
	v_max3_f32 v32, v32, v174, v175
	v_cndmask_b32_e32 v42, v33, v155, vcc
	v_cndmask_b32_e64 v33, v155, v71, s[2:3]
	v_cmp_lt_i32_e64 s[2:3], 15, v157
	v_max3_f32 v32, v32, v176, v51
	v_cndmask_b32_e32 v40, v33, v155, vcc
	v_cndmask_b32_e64 v33, v155, v72, s[2:3]
	v_cmp_lt_i32_e64 s[2:3], 16, v157
	v_max3_f32 v32, v32, v50, v48
	v_cndmask_b32_e32 v41, v33, v155, vcc
	v_cndmask_b32_e64 v33, v155, v73, s[2:3]
	v_cmp_lt_i32_e64 s[2:3], 17, v157
	v_max3_f32 v32, v32, v49, v45
	v_cndmask_b32_e32 v39, v33, v155, vcc
	v_cndmask_b32_e64 v33, v155, v74, s[2:3]
	v_cmp_lt_i32_e64 s[2:3], 18, v157
	v_max3_f32 v32, v32, v46, v47
	v_cndmask_b32_e32 v38, v33, v155, vcc
	v_cndmask_b32_e64 v33, v155, v75, s[2:3]
	v_cmp_lt_i32_e64 s[2:3], 23, v157
	v_max3_f32 v32, v32, v44, v43
	v_cndmask_b32_e32 v37, v33, v155, vcc
	v_cndmask_b32_e64 v33, v155, v76, s[2:3]
	v_cmp_lt_i32_e64 s[2:3], 24, v157
	v_max3_f32 v32, v32, v42, v40
	v_cndmask_b32_e32 v34, v33, v155, vcc
	v_cndmask_b32_e64 v33, v155, v77, s[2:3]
	v_cmp_lt_i32_e64 s[2:3], 25, v157
	v_max3_f32 v32, v32, v41, v39
	v_cndmask_b32_e32 v35, v33, v155, vcc
	v_cndmask_b32_e64 v33, v155, v78, s[2:3]
	v_cmp_lt_i32_e64 s[2:3], 26, v157
	v_max3_f32 v32, v32, v38, v37
	v_cndmask_b32_e32 v36, v33, v155, vcc
	v_cndmask_b32_e64 v33, v155, v79, s[2:3]
	v_max3_f32 v32, v32, v34, v35
	v_cndmask_b32_e32 v33, v33, v155, vcc
	v_max3_f32 v32, v32, v36, v33
	ds_bpermute_b32 v57, v141, v32
	s_ashr_i32 s15, s14, 31
	s_lshl_b64 s[2:3], s[16:17], 23
	s_lshl_b64 s[14:15], s[14:15], 10
	s_add_u32 s2, s20, s2
	s_waitcnt lgkmcnt(0)
	v_max_f32_e32 v57, v57, v57
	v_max_f32_e32 v32, v32, v57
	v_sub_f32_e32 v0, v0, v32
	v_exp_f32_e32 v0, v0
	v_sub_f32_e32 v1, v1, v32
	v_exp_f32_e32 v1, v1
	v_sub_f32_e32 v2, v2, v32
	v_exp_f32_e32 v2, v2
	v_sub_f32_e32 v3, v3, v32
	v_exp_f32_e32 v3, v3
	v_sub_f32_e32 v4, v4, v32
	v_add_f32_e32 v57, 0, v0
	v_exp_f32_e32 v4, v4
	v_sub_f32_e32 v5, v5, v32
	v_add_f32_e32 v57, v1, v57
	v_exp_f32_e32 v5, v5
	v_sub_f32_e32 v6, v6, v32
	v_add_f32_e32 v57, v2, v57
	v_exp_f32_e32 v6, v6
	v_sub_f32_e32 v7, v7, v32
	v_add_f32_e32 v57, v3, v57
	v_exp_f32_e32 v7, v7
	v_sub_f32_e32 v8, v8, v32
	v_add_f32_e32 v57, v4, v57
	v_exp_f32_e32 v58, v8
	v_sub_f32_e32 v9, v9, v32
	v_add_f32_e32 v8, v5, v57
	v_exp_f32_e32 v57, v9
	v_sub_f32_e32 v9, v10, v32
	v_add_f32_e32 v8, v6, v8
	v_exp_f32_e32 v59, v9
	v_sub_f32_e32 v9, v11, v32
	v_add_f32_e32 v8, v7, v8
	v_exp_f32_e32 v60, v9
	v_sub_f32_e32 v9, v12, v32
	v_add_f32_e32 v8, v58, v8
	v_exp_f32_e32 v12, v9
	v_sub_f32_e32 v9, v13, v32
	v_add_f32_e32 v8, v57, v8
	v_exp_f32_e32 v13, v9
	v_sub_f32_e32 v9, v14, v32
	v_add_f32_e32 v8, v59, v8
	v_exp_f32_e32 v14, v9
	v_sub_f32_e32 v9, v15, v32
	v_add_f32_e32 v8, v60, v8
	v_exp_f32_e32 v15, v9
	v_sub_f32_e32 v9, v16, v32
	v_add_f32_e32 v8, v12, v8
	v_exp_f32_e32 v64, v9
	v_sub_f32_e32 v9, v17, v32
	v_add_f32_e32 v8, v13, v8
	v_exp_f32_e32 v65, v9
	v_sub_f32_e32 v9, v18, v32
	v_add_f32_e32 v8, v14, v8
	v_exp_f32_e32 v66, v9
	v_sub_f32_e32 v9, v19, v32
	v_add_f32_e32 v8, v15, v8
	v_exp_f32_e32 v67, v9
	v_sub_f32_e32 v9, v20, v32
	v_add_f32_e32 v8, v64, v8
	v_exp_f32_e32 v68, v9
	v_sub_f32_e32 v9, v21, v32
	v_add_f32_e32 v8, v65, v8
	v_exp_f32_e32 v69, v9
	v_sub_f32_e32 v9, v22, v32
	v_add_f32_e32 v8, v66, v8
	v_exp_f32_e32 v70, v9
	v_sub_f32_e32 v9, v23, v32
	v_add_f32_e32 v8, v67, v8
	v_exp_f32_e32 v71, v9
	v_sub_f32_e32 v9, v24, v32
	v_add_f32_e32 v8, v68, v8
	v_exp_f32_e32 v72, v9
	v_sub_f32_e32 v9, v25, v32
	v_add_f32_e32 v8, v69, v8
	v_exp_f32_e32 v73, v9
	v_sub_f32_e32 v9, v26, v32
	v_add_f32_e32 v8, v70, v8
	v_exp_f32_e32 v74, v9
	v_sub_f32_e32 v9, v27, v32
	v_add_f32_e32 v8, v71, v8
	v_exp_f32_e32 v75, v9
	v_sub_f32_e32 v9, v28, v32
	v_add_f32_e32 v8, v72, v8
	v_exp_f32_e32 v76, v9
	v_sub_f32_e32 v9, v29, v32
	v_add_f32_e32 v8, v73, v8
	v_exp_f32_e32 v77, v9
	v_sub_f32_e32 v9, v30, v32
	v_add_f32_e32 v8, v74, v8
	v_exp_f32_e32 v78, v9
	v_sub_f32_e32 v9, v31, v32
	v_add_f32_e32 v8, v75, v8
	v_exp_f32_e32 v79, v9
	v_sub_f32_e32 v9, v135, v32
	v_add_f32_e32 v8, v76, v8
	v_exp_f32_e32 v135, v9
	v_sub_f32_e32 v9, v137, v32
	v_add_f32_e32 v8, v77, v8
	v_exp_f32_e32 v137, v9
	v_sub_f32_e32 v9, v113, v32
	v_add_f32_e32 v8, v78, v8
	v_exp_f32_e32 v113, v9
	v_sub_f32_e32 v9, v138, v32
	v_add_f32_e32 v8, v79, v8
	v_exp_f32_e32 v138, v9
	v_sub_f32_e32 v9, v139, v32
	v_add_f32_e32 v8, v135, v8
	v_exp_f32_e32 v139, v9
	v_sub_f32_e32 v9, v158, v32
	v_add_f32_e32 v8, v137, v8
	v_exp_f32_e32 v157, v9
	v_sub_f32_e32 v9, v159, v32
	v_add_f32_e32 v8, v113, v8
	v_exp_f32_e32 v158, v9
	v_sub_f32_e32 v9, v160, v32
	v_add_f32_e32 v8, v138, v8
	v_exp_f32_e32 v159, v9
	v_sub_f32_e32 v9, v161, v32
	v_add_f32_e32 v8, v139, v8
	v_exp_f32_e32 v160, v9
	v_sub_f32_e32 v9, v162, v32
	v_add_f32_e32 v8, v157, v8
	v_exp_f32_e32 v161, v9
	v_sub_f32_e32 v9, v163, v32
	v_add_f32_e32 v8, v158, v8
	v_exp_f32_e32 v162, v9
	v_sub_f32_e32 v9, v164, v32
	v_add_f32_e32 v8, v159, v8
	v_exp_f32_e32 v163, v9
	v_sub_f32_e32 v9, v165, v32
	v_add_f32_e32 v8, v160, v8
	v_exp_f32_e32 v164, v9
	v_sub_f32_e32 v9, v166, v32
	v_add_f32_e32 v8, v161, v8
	v_exp_f32_e32 v165, v9
	v_sub_f32_e32 v9, v167, v32
	v_add_f32_e32 v8, v162, v8
	v_exp_f32_e32 v166, v9
	v_sub_f32_e32 v9, v168, v32
	v_add_f32_e32 v8, v163, v8
	v_exp_f32_e32 v167, v9
	v_sub_f32_e32 v9, v169, v32
	v_add_f32_e32 v8, v164, v8
	v_exp_f32_e32 v168, v9
	v_sub_f32_e32 v9, v170, v32
	v_add_f32_e32 v8, v165, v8
	v_exp_f32_e32 v169, v9
	v_sub_f32_e32 v9, v171, v32
	v_add_f32_e32 v8, v166, v8
	v_exp_f32_e32 v170, v9
	v_sub_f32_e32 v9, v172, v32
	v_add_f32_e32 v8, v167, v8
	v_exp_f32_e32 v171, v9
	v_sub_f32_e32 v9, v52, v32
	v_add_f32_e32 v8, v168, v8
	v_exp_f32_e32 v172, v9
	v_sub_f32_e32 v9, v53, v32
	v_add_f32_e32 v8, v169, v8
	v_exp_f32_e32 v177, v9
	v_sub_f32_e32 v9, v54, v32
	v_add_f32_e32 v8, v170, v8
	v_exp_f32_e32 v178, v9
	v_add3_u32 v9, s36, v146, v145
	v_add_f32_e32 v8, v171, v8
	v_add_u32_e32 v179, 0x6800, v9
	v_add_f32_e32 v8, v172, v8
	v_cvt_pk_bf16_f32 v0, v0, v1
	v_cvt_pk_bf16_f32 v1, v2, v3
	v_cvt_pk_bf16_f32 v2, v4, v5
	v_cvt_pk_bf16_f32 v3, v6, v7
	ds_read2_b64 v[4:7], v179 offset0:128 offset1:130
	v_add_f32_e32 v8, v177, v8
	v_add_f32_e32 v52, v178, v8
	v_sub_f32_e32 v8, v55, v32
	v_exp_f32_e32 v180, v8
	v_sub_f32_e32 v8, v56, v32
	v_add_u32_e32 v182, 0x9800, v9
	v_exp_f32_e32 v181, v8
	ds_read2_b64 v[8:11], v182 offset0:192 offset1:194
	s_waitcnt lgkmcnt(1)
	v_mfma_f32_32x32x16_bf16 v[16:31], v[4:7], v[0:3], 0
	v_add_f32_e32 v4, v180, v52
	v_cvt_pk_bf16_f32 v52, v58, v57
	v_cvt_pk_bf16_f32 v53, v59, v60
	v_sub_f32_e32 v60, v173, v32
	v_cvt_pk_bf16_f32 v54, v12, v13
	v_cvt_pk_bf16_f32 v55, v14, v15
	ds_read2_b64 v[56:59], v179 offset0:132 offset1:134
	v_exp_f32_e32 v173, v60
	v_sub_f32_e32 v60, v174, v32
	v_exp_f32_e32 v174, v60
	v_sub_f32_e32 v60, v175, v32
	v_exp_f32_e32 v175, v60
	ds_read2_b64 v[60:63], v182 offset0:196 offset1:198
	v_add_f32_e32 v183, v181, v4
	s_waitcnt lgkmcnt(2)
	v_mfma_f32_32x32x16_bf16 v[0:15], v[8:11], v[0:3], 0
	v_sub_f32_e32 v51, v51, v32
	v_sub_f32_e32 v50, v50, v32
	v_sub_f32_e32 v48, v48, v32
	v_sub_f32_e32 v45, v45, v32
	v_sub_f32_e32 v44, v44, v32
	v_sub_f32_e32 v43, v43, v32
	v_sub_f32_e32 v42, v42, v32
	s_waitcnt lgkmcnt(1)
	v_mfma_f32_32x32x16_bf16 v[16:31], v[56:59], v[52:55], v[16:31]
	v_sub_f32_e32 v56, v176, v32
	v_exp_f32_e32 v176, v56
	v_cvt_pk_bf16_f32 v56, v64, v65
	v_cvt_pk_bf16_f32 v57, v66, v67
	v_cvt_pk_bf16_f32 v58, v68, v69
	v_cvt_pk_bf16_f32 v59, v70, v71
	ds_read2_b64 v[64:67], v179 offset0:136 offset1:138
	s_waitcnt lgkmcnt(1)
	v_mfma_f32_32x32x16_bf16 v[0:15], v[60:63], v[52:55], v[0:15]
	v_add_f32_e32 v52, v173, v183
	v_add_f32_e32 v52, v174, v52
	v_add_f32_e32 v52, v175, v52
	v_add_f32_e32 v68, v176, v52
	ds_read2_b64 v[52:55], v182 offset0:200 offset1:202
	v_exp_f32_e32 v69, v51
	v_exp_f32_e32 v70, v50
	s_waitcnt lgkmcnt(1)
	v_mfma_f32_32x32x16_bf16 v[16:31], v[64:67], v[56:59], v[16:31]
	v_cvt_pk_bf16_f32 v60, v72, v73
	v_cvt_pk_bf16_f32 v61, v74, v75
	v_cvt_pk_bf16_f32 v62, v76, v77
	v_cvt_pk_bf16_f32 v63, v78, v79
	ds_read2_b64 v[64:67], v179 offset0:140 offset1:142
	v_add_f32_e32 v50, v69, v68
	v_exp_f32_e32 v68, v48
	v_sub_f32_e32 v48, v49, v32
	s_waitcnt lgkmcnt(1)
	v_mfma_f32_32x32x16_bf16 v[0:15], v[52:55], v[56:59], v[0:15]
	v_add_f32_e32 v52, v70, v50
	v_exp_f32_e32 v71, v48
	ds_read2_b64 v[48:51], v182 offset0:204 offset1:206
	v_add_f32_e32 v52, v68, v52
	v_exp_f32_e32 v72, v44
	v_exp_f32_e32 v73, v43
	v_sub_f32_e32 v40, v40, v32
	s_waitcnt lgkmcnt(1)
	v_mfma_f32_32x32x16_bf16 v[16:31], v[64:67], v[60:63], v[16:31]
	v_add_f32_e32 v64, v71, v52
	v_cvt_pk_bf16_f32 v52, v135, v137
	v_cvt_pk_bf16_f32 v53, v113, v138
	v_cvt_pk_bf16_f32 v54, v139, v157
	v_cvt_pk_bf16_f32 v55, v158, v159
	ds_read2_b64 v[56:59], v179 offset0:144 offset1:146
	v_exp_f32_e32 v65, v45
	v_sub_f32_e32 v45, v46, v32
	s_waitcnt lgkmcnt(1)
	v_mfma_f32_32x32x16_bf16 v[0:15], v[48:51], v[60:63], v[0:15]
	v_exp_f32_e32 v66, v45
	v_sub_f32_e32 v45, v47, v32
	ds_read2_b64 v[46:49], v182 offset0:208 offset1:210
	v_exp_f32_e32 v67, v45
	v_add_f32_e32 v44, v65, v64
	v_add_f32_e32 v44, v66, v44
	v_sub_f32_e32 v39, v39, v32
	s_waitcnt lgkmcnt(1)
	v_mfma_f32_32x32x16_bf16 v[16:31], v[56:59], v[52:55], v[16:31]
	v_cvt_pk_bf16_f32 v56, v160, v161
	v_cvt_pk_bf16_f32 v57, v162, v163
	v_cvt_pk_bf16_f32 v58, v164, v165
	v_cvt_pk_bf16_f32 v59, v166, v167
	ds_read2_b64 v[60:63], v179 offset0:148 offset1:150
	v_add_f32_e32 v44, v67, v44
	v_add_f32_e32 v64, v72, v44
	s_waitcnt lgkmcnt(1)
	v_mfma_f32_32x32x16_bf16 v[0:15], v[46:49], v[52:55], v[0:15]
	ds_read2_b64 v[44:47], v182 offset0:212 offset1:214
	v_cvt_pk_bf16_f32 v48, v168, v169
	v_cvt_pk_bf16_f32 v49, v170, v171
	v_cvt_pk_bf16_f32 v50, v172, v177
	v_cvt_pk_bf16_f32 v51, v178, v180
	ds_read2_b64 v[52:55], v179 offset0:152 offset1:154
	v_sub_f32_e32 v38, v38, v32
	s_waitcnt lgkmcnt(2)
	v_mfma_f32_32x32x16_bf16 v[16:31], v[60:63], v[56:59], v[16:31]
	v_exp_f32_e32 v60, v42
	v_add_f32_e32 v42, v73, v64
	v_sub_f32_e32 v34, v34, v32
	v_sub_f32_e32 v37, v37, v32
	v_exp_f32_e32 v61, v37
	v_sub_f32_e32 v33, v33, v32
	v_exp_f32_e32 v33, v33
	s_waitcnt lgkmcnt(1)
	v_mfma_f32_32x32x16_bf16 v[0:15], v[44:47], v[56:59], v[0:15]
	v_exp_f32_e32 v57, v40
	v_sub_f32_e32 v40, v41, v32
	v_add_f32_e32 v56, v60, v42
	v_exp_f32_e32 v58, v40
	ds_read2_b64 v[40:43], v182 offset0:216 offset1:218
	v_exp_f32_e32 v59, v39
	v_cvt_pk_bf16_f32 v44, v181, v173
	s_waitcnt lgkmcnt(0)
	v_mfma_f32_32x32x16_bf16 v[0:15], v[40:43], v[48:51], v[0:15]
	v_exp_f32_e32 v42, v38
	v_add_f32_e32 v38, v57, v56
	v_add_f32_e32 v38, v58, v38
	v_add_f32_e32 v38, v59, v38
	v_cvt_pk_bf16_f32 v45, v174, v175
	v_cvt_pk_bf16_f32 v46, v176, v69
	v_cvt_pk_bf16_f32 v47, v70, v68
	v_mfma_f32_32x32x16_bf16 v[16:31], v[52:55], v[48:51], v[16:31]
	ds_read2_b64 v[52:55], v179 offset0:156 offset1:158
	v_add_f32_e32 v56, v42, v38
	ds_read2_b64 v[38:41], v182 offset0:220 offset1:222
	v_cvt_pk_bf16_f32 v48, v71, v65
	v_cvt_pk_bf16_f32 v49, v66, v67
	v_cvt_pk_bf16_f32 v50, v72, v73
	v_cvt_pk_bf16_f32 v51, v60, v57
	s_waitcnt lgkmcnt(1)
	v_mfma_f32_32x32x16_bf16 v[16:31], v[52:55], v[44:47], v[16:31]
	ds_read2_b64 v[52:55], v179 offset0:160 offset1:162
	s_addc_u32 s3, s21, s3
	s_add_u32 s2, s2, s14
	s_addc_u32 s3, s3, s15
	s_lshl_b32 s6, s8, 6
	s_ashr_i32 s8, s6, 31
	s_add_u32 s2, s2, s6
	s_waitcnt lgkmcnt(1)
	v_mfma_f32_32x32x16_bf16 v[0:15], v[38:41], v[44:47], v[0:15]
	v_exp_f32_e32 v46, v34
	v_sub_f32_e32 v34, v35, v32
	v_exp_f32_e32 v47, v34
	v_sub_f32_e32 v34, v36, v32
	v_exp_f32_e32 v57, v34
	ds_read2_b64 v[34:37], v182 offset0:224 offset1:226
	v_cvt_pk_bf16_f32 v38, v58, v59
	v_cvt_pk_bf16_f32 v39, v42, v61
	v_cvt_pk_bf16_f32 v40, v46, v47
	v_cvt_pk_bf16_f32 v41, v57, v33
	ds_read2_b64 v[42:45], v179 offset0:164 offset1:166
	s_waitcnt lgkmcnt(2)
	v_mfma_f32_32x32x16_bf16 v[16:31], v[52:55], v[48:51], v[16:31]
	s_addc_u32 s3, s3, s8
	s_andn2_b64 vcc, exec, s[12:13]
	s_xor_b32 s34, s34, 1
	s_waitcnt lgkmcnt(1)
	v_mfma_f32_32x32x16_bf16 v[0:15], v[34:37], v[48:51], v[0:15]
	v_add_f32_e32 v34, v61, v56
	v_add_f32_e32 v34, v46, v34
	v_add_f32_e32 v34, v47, v34
	v_add_f32_e32 v34, v57, v34
	v_add_f32_e32 v36, v33, v34
	ds_bpermute_b32 v37, v141, v36
	v_fma_f32 v46, v156, s31, -v32
	s_waitcnt lgkmcnt(1)
	v_mfma_f32_32x32x16_bf16 v[16:31], v[42:45], v[38:41], v[16:31]
	ds_read2_b64 v[32:35], v182 offset0:228 offset1:230
	v_exp_f32_e32 v42, v46
	s_waitcnt lgkmcnt(1)
	v_add_f32_e32 v36, v36, v37
	v_add_f32_e32 v36, v42, v36
	v_rcp_f32_e32 v36, v36
	s_waitcnt lgkmcnt(0)
	v_mfma_f32_32x32x16_bf16 v[0:15], v[32:35], v[38:41], v[0:15]
	v_mul_f32_e32 v32, 0x41000000, v36
	s_nop 2
	v_mul_f32_e32 v16, v32, v16
	v_mul_f32_e32 v17, v32, v17
	v_mov_b32_e32 v33, v112
	v_cvt_pk_fp8_f32 v33, v16, v17
	v_mul_f32_e32 v16, v32, v20
	v_mul_f32_e32 v17, v32, v21
	v_mov_b32_e32 v20, v112
	v_cvt_pk_fp8_f32 v20, v16, v17
	v_mul_f32_e32 v16, v32, v22
	v_mul_f32_e32 v17, v32, v23
	v_mov_b32_e32 v21, v112
	v_cvt_pk_fp8_f32 v20, v16, v17 op_sel:[0,0,1]
	v_mul_f32_e32 v16, v32, v24
	v_mul_f32_e32 v17, v32, v25
	v_cvt_pk_fp8_f32 v21, v16, v17
	v_mul_f32_e32 v16, v32, v28
	v_mul_f32_e32 v17, v32, v29
	v_mov_b32_e32 v22, v112
	v_cvt_pk_fp8_f32 v22, v16, v17
	v_mul_f32_e32 v16, v32, v30
	v_mul_f32_e32 v17, v32, v31
	v_mul_f32_e32 v0, v32, v0
	v_cvt_pk_fp8_f32 v22, v16, v17 op_sel:[0,0,1]
	v_mul_f32_e32 v1, v32, v1
	v_mov_b32_e32 v16, v112
	v_cvt_pk_fp8_f32 v16, v0, v1
	v_mul_f32_e32 v0, v32, v4
	v_mul_f32_e32 v1, v32, v5
	v_mov_b32_e32 v4, v112
	v_cvt_pk_fp8_f32 v4, v0, v1
	v_mul_f32_e32 v0, v32, v6
	v_mul_f32_e32 v1, v32, v7
	v_mov_b32_e32 v5, v112
	v_cvt_pk_fp8_f32 v4, v0, v1 op_sel:[0,0,1]
	v_mul_f32_e32 v0, v32, v8
	v_mul_f32_e32 v1, v32, v9
	v_cvt_pk_fp8_f32 v5, v0, v1
	v_mul_f32_e32 v0, v32, v12
	v_mul_f32_e32 v1, v32, v13
	v_mov_b32_e32 v6, v112
	v_mul_f32_e32 v18, v32, v18
	v_mul_f32_e32 v19, v32, v19
	v_cvt_pk_fp8_f32 v6, v0, v1
	v_cvt_pk_fp8_f32 v33, v18, v19 op_sel:[0,0,1]
	v_mul_f32_e32 v18, v32, v26
	v_mul_f32_e32 v19, v32, v27
	v_cvt_pk_fp8_f32 v21, v18, v19 op_sel:[0,0,1]
	v_mul_f32_e32 v2, v32, v2
	v_mul_f32_e32 v3, v32, v3
	v_cvt_pk_fp8_f32 v16, v2, v3 op_sel:[0,0,1]
	v_mul_f32_e32 v2, v32, v10
	v_mul_f32_e32 v3, v32, v11
	v_mul_f32_e32 v0, v32, v14
	v_mul_f32_e32 v1, v32, v15
	v_cvt_pk_fp8_f32 v5, v2, v3 op_sel:[0,0,1]
	v_cvt_pk_fp8_f32 v6, v0, v1 op_sel:[0,0,1]
	ds_write2_b32 v153, v33, v20 offset1:2
	ds_write2_b32 v153, v21, v22 offset0:4 offset1:6
	ds_write2_b32 v153, v16, v4 offset0:8 offset1:10
	ds_write2_b32 v153, v5, v6 offset0:12 offset1:14
	s_waitcnt lgkmcnt(0)
	ds_read_b128 v[0:3], v154
	ds_read_b128 v[4:7], v154 offset:2304
	v_lshl_add_u64 v[8:9], s[2:3], 0, v[128:129]
	v_lshl_add_u64 v[10:11], v[8:9], 0, v[130:131]
	s_waitcnt lgkmcnt(1)
	global_store_dwordx4 v[10:11], v[0:3], off
	s_nop 1
	v_lshl_add_u64 v[0:1], v[8:9], 0, v[132:133]
	s_waitcnt lgkmcnt(0)
	global_store_dwordx4 v[0:1], v[4:7], off
	s_cbranch_vccnz .LBB0_868
	s_mul_i32 s2, s34, 0xd000
	s_add_i32 s2, s2, 0
	v_add_u32_e32 v0, s2, v142
	v_add_u32_e32 v2, v0, v147
	v_add_u32_e32 v1, v0, v143
	s_waitcnt vmcnt(2)
	ds_write_b128 v2, v[80:83]
	ds_write_b128 v1, v[84:87] offset:27648
	v_add_u32_e32 v2, v0, v148
	v_add_u32_e32 v0, v0, v149
	ds_write_b128 v2, v[88:91]
	ds_write_b128 v1, v[108:111] offset:27776
	ds_write_b128 v0, v[114:117]
	ds_write_b128 v1, v[118:121] offset:27904
	s_branch .LBB0_868
